# final + FILL_E 4 instead of 8
# baseline (speedup 1.0000x reference)
.LBB0_1641:
	s_mul_i32 s2, s76, 0xd760
	s_add_i32 s2, s2, 0xc300
	s_sub_i32 s82, s11, s4
	s_max_i32 s57, s50, s2
	s_mul_i32 s2, s82, 0x100
	s_add_i32 s2, s2, s57
	s_min_i32 s50, s2, 0x34920
	s_cmp_lt_i32 s74, 0
	s_mov_b64 s[2:3], -1
	s_cbranch_scc0 .LBB0_2087
	s_ashr_i32 s9, s10, 6
	s_not_b32 s83, s74
	s_lshl_b32 s3, s9, 3
	s_lshl_b32 s2, s83, 6
	s_add_i32 s54, s57, s3
	s_add_i32 s42, s54, s2
	s_cmp_lt_i32 s42, s50
	s_cselect_b32 s77, s42, -1
	s_cmp_lt_i32 s77, 0
	v_and_b32_e32 v132, 63, v1
	s_cbranch_scc1 .LBB0_1654
	s_mul_hi_u32 s2, s77, 0x9824d8ed
	s_lshr_b32 s2, s2, 15
	s_mul_i32 s3, s2, 0xd760
	s_sub_i32 s24, s77, s3
	s_cmpk_gt_u32 s24, 0xc2ff
	s_mov_b64 s[20:21], -1
	s_cbranch_scc0 .LBB0_1675
	s_add_i32 s20, s2, 1
	s_add_i32 s3, s24, 0xffff3d00
	s_cmpk_lt_u32 s3, 0x1400
	s_cselect_b32 s3, s3, s24
	s_cmpk_gt_u32 s3, 0xbff
	s_mov_b64 s[22:23], -1
	s_cbranch_scc0 .LBB0_1672
	s_cmpk_gt_u32 s3, 0x13ff
	s_cbranch_scc0 .LBB0_1669
	s_add_u32 s25, s78, 0x6200000
	s_addc_u32 s26, s79, 0
	s_cmpk_gt_u32 s3, 0x93ff
	s_cbranch_scc0 .LBB0_1666
	s_add_u32 s27, s78, 0x26a00000
	s_addc_u32 s28, s79, 0
	s_cmpk_gt_u32 s3, 0xd3ff
	s_cbranch_scc0 .LBB0_1663
	s_cmpk_gt_u32 s3, 0xd5ff
	s_cbranch_scc0 .LBB0_1660
	s_cmpk_gt_u32 s3, 0xd6ff
	s_cbranch_scc0 .LBB0_1657
	s_lshl_b32 s22, s3, 5
	s_cmpk_gt_u32 s3, 0xd71f
	s_mov_b64 s[18:19], -1
	s_cbranch_scc0 .LBB0_1652
	s_mov_b32 s21, s47
	v_readlane_b32 s56, v243, 40
	s_lshl_b64 s[10:11], s[20:21], 19
	v_readlane_b32 s62, v243, 46
	v_readlane_b32 s63, v243, 47
	s_add_u32 s16, s62, s10
	s_addc_u32 s17, s63, s11
	s_lshl_b64 s[10:11], s[20:21], 18
	s_add_u32 s8, s78, s10
	s_addc_u32 s13, s79, s11
	s_add_u32 s10, s8, 0x37000000
	s_addc_u32 s11, s13, 0
	s_add_u32 s12, s8, 0x37100000
	v_readlane_b32 s58, v243, 42
	s_addc_u32 s13, s13, 0
	s_lshl_b32 s8, s20, 13
	v_readlane_b32 s59, v243, 43
	s_add_u32 s14, s58, s8
	s_addc_u32 s15, s59, 0
	s_and_b32 s8, s22, 0x7fffffc0
	v_readlane_b32 s57, v243, 41
	v_readlane_b32 s60, v243, 44
	v_readlane_b32 s61, v243, 45
	v_readlane_b32 s64, v243, 48
	v_readlane_b32 s65, v243, 49
	v_readlane_b32 s66, v243, 50
	v_readlane_b32 s67, v243, 51
	v_readlane_b32 s68, v243, 52
	v_readlane_b32 s69, v243, 53
	v_readlane_b32 s70, v243, 54
	v_readlane_b32 s71, v243, 55
	s_add_i32 s8, s8, 0xffe51c00
	s_and_b32 s89, s22, 32
	s_mov_b64 s[18:19], 0
